# batched the per-row loads of the diff/sub-norm phase behind counted vmcnt waits
# speedup vs baseline: 1.0089x; 1.0035x over previous
; __device__ __forceinline__ unsigned cvt4_fp8(float a, float b, float c, float d) { int w = 0; w = __builtin_amdgcn_cvt_pk_fp8_f32(a, b, w, false); w = __builtin_amdgcn_cvt_pk_fp8_f32(c, d, w, true); return (unsigned)w; }
; __device__ __forceinline__ void diff_phase(Frame& F) {
;     ...
;     for (int r = gw; r < NX; r += NGW) {
; #pragma unroll
;         for (int h = 0; h < 4; ++h) {
;             const u32x2 a = *(const u32x2*)(OBR + (size_t)r * at::LDO + h * 512 + 4 * lane), c = *(const u32x2*)(OBR + (size_t)r * at::LDO + h * 512 + 256 + 4 * lane);
;             f32x4 d;
;             d[0] = __uint_as_float(a.x << 16) - lam * __uint_as_float(c.x << 16); d[1] = __uint_as_float(a.x & 0xffff0000u) - lam * __uint_as_float(c.x & 0xffff0000u);
;             d[2] = __uint_as_float(a.y << 16) - lam * __uint_as_float(c.y << 16); d[3] = __uint_as_float(a.y & 0xffff0000u) - lam * __uint_as_float(c.y & 0xffff0000u);
;             const float ss = wave_sum((d[0] * d[0] + d[1] * d[1]) + (d[2] * d[2] + d[3] * d[3]));
;             const float rs = 0.8f / sqrtf(ss * (1.0f / 256.0f) + EPS);
;             *(unsigned*)(OB8 + (size_t)r * D + h * 256 + 4 * lane) = cvt4_fp8(d[0] * rs * g4[0], d[1] * rs * g4[1], d[2] * rs * g4[2], d[3] * rs * g4[3]);
;         }
;     }
.LBB0_1817:
	v_lshl_add_u64 v[8:9], s[70:71], 0, v[4:5]
	v_lshl_add_u64 v[22:23], s[70:71], 0, v[6:7]
	v_add_co_u32_e64 v8, s[0:1], s10, v8
	v_add_co_u32_e32 v24, vcc, 0x8fbe7000, v22
	s_nop 0
	v_addc_co_u32_e64 v9, s[0:1], 0, v9, s[0:1]
	v_add_co_u32_e64 v10, s[0:1], s11, v22
	v_addc_co_u32_e32 v25, vcc, 0, v23, vcc
	s_nop 0
	v_addc_co_u32_e64 v11, s[0:1], 0, v23, s[0:1]
	global_load_dwordx2 v[40:41], v[24:25], off offset:2048
	global_load_dwordx2 v[42:43], v[24:25], off offset:2560
	global_load_dwordx2 v[44:45], v[24:25], off offset:3072
	global_load_dwordx2 v[46:47], v[24:25], off offset:3584
	global_load_dwordx2 v[48:49], v[10:11], off
	global_load_dwordx2 v[50:51], v[10:11], off offset:512
	global_load_dwordx2 v[52:53], v[10:11], off offset:1024
	global_load_dwordx2 v[54:55], v[10:11], off offset:1536
	v_mov_b32_e32 v28, 0
	v_mov_b32_e32 v29, 0
	s_add_i32 s2, s2, s4
	v_lshl_add_u64 v[4:5], v[4:5], 0, s[6:7]
	v_lshl_add_u64 v[6:7], v[6:7], 0, s[8:9]
	s_cmpk_lt_i32 s2, 0x4000
	s_waitcnt vmcnt(7)
	v_lshlrev_b32_e32 v30, 16, v40
	s_waitcnt vmcnt(6)
	v_lshlrev_b32_e32 v31, 16, v42
	v_and_b32_e32 v22, 0xffff0000, v40
	v_and_b32_e32 v26, 0xffff0000, v42
	v_lshlrev_b32_e32 v32, 16, v41
	v_lshlrev_b32_e32 v33, 16, v43
	v_and_b32_e32 v23, 0xffff0000, v41
	v_and_b32_e32 v27, 0xffff0000, v43
	v_fma_f32 v22, -v19, v26, v22
	v_fma_f32 v23, -v19, v27, v23
	v_fma_f32 v30, -v19, v31, v30
	v_fma_f32 v26, -v19, v33, v32
	v_mul_f32_e32 v27, v22, v22
	v_mul_f32_e32 v31, v23, v23
	v_fmac_f32_e32 v27, v30, v30
	v_fmac_f32_e32 v31, v26, v26
	v_add_f32_e32 v27, v27, v31
	ds_bpermute_b32 v31, v13, v27
	s_waitcnt lgkmcnt(0)
	v_add_f32_e32 v27, v27, v31
	ds_bpermute_b32 v31, v14, v27
	s_waitcnt lgkmcnt(0)
	v_add_f32_e32 v27, v27, v31
	ds_bpermute_b32 v31, v15, v27
	s_waitcnt lgkmcnt(0)
	v_add_f32_e32 v27, v27, v31
	ds_bpermute_b32 v31, v16, v27
	s_waitcnt lgkmcnt(0)
	v_add_f32_e32 v27, v27, v31
	ds_bpermute_b32 v31, v17, v27
	s_waitcnt lgkmcnt(0)
	v_add_f32_e32 v27, v27, v31
	ds_bpermute_b32 v31, v18, v27
	s_waitcnt lgkmcnt(0)
	v_add_f32_e32 v27, v27, v31
	v_fmamk_f32 v27, v27, 0x3b800000, v20
	v_mul_f32_e32 v31, 0x4f800000, v27
	v_cmp_gt_f32_e32 vcc, s3, v27
	s_nop 1
	v_cndmask_b32_e32 v27, v27, v31, vcc
	v_sqrt_f32_e32 v31, v27
	s_nop 0
	v_add_u32_e32 v32, -1, v31
	v_add_u32_e32 v33, 1, v31
	v_fma_f32 v34, -v32, v31, v27
	v_fma_f32 v35, -v33, v31, v27
	v_cmp_ge_f32_e64 s[0:1], 0, v34
	s_nop 1
	v_cndmask_b32_e64 v31, v31, v32, s[0:1]
	v_cmp_lt_f32_e64 s[0:1], 0, v35
	s_nop 1
	v_cndmask_b32_e64 v31, v31, v33, s[0:1]
	v_mul_f32_e32 v32, 0x37800000, v31
	v_cndmask_b32_e32 v31, v31, v32, vcc
	v_cmp_class_f32_e32 vcc, v27, v21
	s_nop 1
	v_cndmask_b32_e32 v27, v31, v27, vcc
	v_div_scale_f32 v31, s[0:1], v27, v27, s5
	v_rcp_f32_e32 v33, v31
	v_div_scale_f32 v32, vcc, s5, v27, s5
	v_fma_f32 v34, -v31, v33, 1.0
	v_fmac_f32_e32 v33, v34, v33
	v_mul_f32_e32 v34, v32, v33
	v_fma_f32 v35, -v31, v34, v32
	v_fmac_f32_e32 v34, v35, v33
	v_fma_f32 v31, -v31, v34, v32
	v_div_fmas_f32 v31, v31, v33, v34
	v_div_fixup_f32 v27, v31, v27, s5
	v_mul_f32_e32 v30, v30, v27
	v_mul_f32_e32 v22, v22, v27
	v_mul_f32_e32 v26, v26, v27
	v_mul_f32_e32 v23, v23, v27
	v_mul_f32_e32 v27, v0, v30
	v_mul_f32_e32 v22, v1, v22
	v_cvt_pk_fp8_f32 v28, v27, v22
	v_mul_f32_e32 v26, v2, v26
	v_mul_f32_e32 v23, v3, v23
	v_cvt_pk_fp8_f32 v28, v26, v23 op_sel:[0,0,1]
	global_store_dword v[8:9], v28, off offset:1024
	s_waitcnt vmcnt(6)
	v_lshlrev_b32_e32 v24, 16, v44
	s_waitcnt vmcnt(5)
	v_lshlrev_b32_e32 v25, 16, v46
	v_and_b32_e32 v22, 0xffff0000, v44
	v_and_b32_e32 v26, 0xffff0000, v46
	v_lshlrev_b32_e32 v28, 16, v45
	v_lshlrev_b32_e32 v30, 16, v47
	v_and_b32_e32 v23, 0xffff0000, v45
	v_and_b32_e32 v27, 0xffff0000, v47
	v_fma_f32 v22, -v19, v26, v22
	v_fma_f32 v23, -v19, v27, v23
	v_fma_f32 v24, -v19, v25, v24
	v_fma_f32 v25, -v19, v30, v28
	v_mul_f32_e32 v26, v22, v22
	v_mul_f32_e32 v27, v23, v23
	v_fmac_f32_e32 v26, v24, v24
	v_fmac_f32_e32 v27, v25, v25
	v_add_f32_e32 v26, v26, v27
	ds_bpermute_b32 v27, v13, v26
	s_waitcnt lgkmcnt(0)
	v_add_f32_e32 v26, v26, v27
	ds_bpermute_b32 v27, v14, v26
	s_waitcnt lgkmcnt(0)
	v_add_f32_e32 v26, v26, v27
	ds_bpermute_b32 v27, v15, v26
	s_waitcnt lgkmcnt(0)
	v_add_f32_e32 v26, v26, v27
	ds_bpermute_b32 v27, v16, v26
	s_waitcnt lgkmcnt(0)
	v_add_f32_e32 v26, v26, v27
	ds_bpermute_b32 v27, v17, v26
	s_waitcnt lgkmcnt(0)
	v_add_f32_e32 v26, v26, v27
	ds_bpermute_b32 v27, v18, v26
	s_waitcnt lgkmcnt(0)
	v_add_f32_e32 v26, v26, v27
	v_fmamk_f32 v26, v26, 0x3b800000, v20
	v_mul_f32_e32 v27, 0x4f800000, v26
	v_cmp_gt_f32_e32 vcc, s3, v26
	s_nop 1
	v_cndmask_b32_e32 v26, v26, v27, vcc
	v_sqrt_f32_e32 v27, v26
	s_nop 0
	v_add_u32_e32 v28, -1, v27
	v_add_u32_e32 v30, 1, v27
	v_fma_f32 v31, -v28, v27, v26
	v_fma_f32 v32, -v30, v27, v26
	v_cmp_ge_f32_e64 s[0:1], 0, v31
	s_nop 1
	v_cndmask_b32_e64 v27, v27, v28, s[0:1]
	v_cmp_lt_f32_e64 s[0:1], 0, v32
	s_nop 1
	v_cndmask_b32_e64 v27, v27, v30, s[0:1]
	v_mul_f32_e32 v28, 0x37800000, v27
	v_cndmask_b32_e32 v27, v27, v28, vcc
	v_cmp_class_f32_e32 vcc, v26, v21
	s_nop 1
	v_cndmask_b32_e32 v26, v27, v26, vcc
	v_div_scale_f32 v27, s[0:1], v26, v26, s5
	v_rcp_f32_e32 v30, v27
	v_div_scale_f32 v28, vcc, s5, v26, s5
	v_fma_f32 v31, -v27, v30, 1.0
	v_fmac_f32_e32 v30, v31, v30
	v_mul_f32_e32 v31, v28, v30
	v_fma_f32 v32, -v27, v31, v28
	v_fmac_f32_e32 v31, v32, v30
	v_fma_f32 v27, -v27, v31, v28
	v_div_fmas_f32 v27, v27, v30, v31
	v_div_fixup_f32 v26, v27, v26, s5
	v_mul_f32_e32 v24, v24, v26
	v_mul_f32_e32 v22, v22, v26
	v_mul_f32_e32 v24, v0, v24
	v_mul_f32_e32 v22, v1, v22
	v_cvt_pk_fp8_f32 v29, v24, v22
	v_mul_f32_e32 v25, v25, v26
	v_mul_f32_e32 v23, v23, v26
	v_mul_f32_e32 v25, v2, v25
	v_mul_f32_e32 v23, v3, v23
	v_cvt_pk_fp8_f32 v29, v25, v23 op_sel:[0,0,1]
	v_mov_b32_e32 v26, 0
	global_store_dword v[8:9], v29, off offset:1280
	s_waitcnt vmcnt(5)
; __device__ __forceinline__ unsigned cvt4_fp8(float a, float b, float c, float d) { int w = 0; w = __builtin_amdgcn_cvt_pk_fp8_f32(a, b, w, false); w = __builtin_amdgcn_cvt_pk_fp8_f32(c, d, w, true); return (unsigned)w; }
; __device__ __forceinline__ void diff_phase(Frame& F) {
;     ...
;     for (int r = gw; r < NX; r += NGW) {
; #pragma unroll
;         for (int h = 0; h < 4; ++h) {
;             const u32x2 a = *(const u32x2*)(OBR + (size_t)r * at::LDO + h * 512 + 4 * lane), c = *(const u32x2*)(OBR + (size_t)r * at::LDO + h * 512 + 256 + 4 * lane);
;             f32x4 d;
;             d[0] = __uint_as_float(a.x << 16) - lam * __uint_as_float(c.x << 16); d[1] = __uint_as_float(a.x & 0xffff0000u) - lam * __uint_as_float(c.x & 0xffff0000u);
;             d[2] = __uint_as_float(a.y << 16) - lam * __uint_as_float(c.y << 16); d[3] = __uint_as_float(a.y & 0xffff0000u) - lam * __uint_as_float(c.y & 0xffff0000u);
;             const float ss = wave_sum((d[0] * d[0] + d[1] * d[1]) + (d[2] * d[2] + d[3] * d[3]));
;             const float rs = 0.8f / sqrtf(ss * (1.0f / 256.0f) + EPS);
;             *(unsigned*)(OB8 + (size_t)r * D + h * 256 + 4 * lane) = cvt4_fp8(d[0] * rs * g4[0], d[1] * rs * g4[1], d[2] * rs * g4[2], d[3] * rs * g4[3]);
;         }
;     }
	v_lshlrev_b32_e32 v27, 16, v48
	s_waitcnt vmcnt(4)
	v_lshlrev_b32_e32 v28, 16, v50
	v_and_b32_e32 v22, 0xffff0000, v48
	v_and_b32_e32 v24, 0xffff0000, v50
	v_lshlrev_b32_e32 v29, 16, v49
	v_lshlrev_b32_e32 v30, 16, v51
	v_and_b32_e32 v23, 0xffff0000, v49
	v_and_b32_e32 v25, 0xffff0000, v51
	v_fma_f32 v22, -v19, v24, v22
	v_fma_f32 v23, -v19, v25, v23
	v_fma_f32 v27, -v19, v28, v27
	v_fma_f32 v24, -v19, v30, v29
	v_mul_f32_e32 v25, v22, v22
	v_mul_f32_e32 v28, v23, v23
	v_fmac_f32_e32 v25, v27, v27
	v_fmac_f32_e32 v28, v24, v24
	v_add_f32_e32 v25, v25, v28
	ds_bpermute_b32 v28, v13, v25
	s_waitcnt lgkmcnt(0)
	v_add_f32_e32 v25, v25, v28
	ds_bpermute_b32 v28, v14, v25
	s_waitcnt lgkmcnt(0)
	v_add_f32_e32 v25, v25, v28
	ds_bpermute_b32 v28, v15, v25
	s_waitcnt lgkmcnt(0)
	v_add_f32_e32 v25, v25, v28
	ds_bpermute_b32 v28, v16, v25
	s_waitcnt lgkmcnt(0)
	v_add_f32_e32 v25, v25, v28
	ds_bpermute_b32 v28, v17, v25
	s_waitcnt lgkmcnt(0)
	v_add_f32_e32 v25, v25, v28
	ds_bpermute_b32 v28, v18, v25
	s_waitcnt lgkmcnt(0)
	v_add_f32_e32 v25, v25, v28
	v_fmamk_f32 v25, v25, 0x3b800000, v20
	v_mul_f32_e32 v28, 0x4f800000, v25
	v_cmp_gt_f32_e32 vcc, s3, v25
	s_nop 1
	v_cndmask_b32_e32 v25, v25, v28, vcc
	v_sqrt_f32_e32 v28, v25
	s_nop 0
	v_add_u32_e32 v29, -1, v28
	v_add_u32_e32 v30, 1, v28
	v_fma_f32 v31, -v29, v28, v25
	v_fma_f32 v32, -v30, v28, v25
	v_cmp_ge_f32_e64 s[0:1], 0, v31
	s_nop 1
	v_cndmask_b32_e64 v28, v28, v29, s[0:1]
	v_cmp_lt_f32_e64 s[0:1], 0, v32
	s_nop 1
	v_cndmask_b32_e64 v28, v28, v30, s[0:1]
	v_mul_f32_e32 v29, 0x37800000, v28
	v_cndmask_b32_e32 v28, v28, v29, vcc
	v_cmp_class_f32_e32 vcc, v25, v21
	s_nop 1
	v_cndmask_b32_e32 v25, v28, v25, vcc
	v_div_scale_f32 v28, s[0:1], v25, v25, s5
	v_rcp_f32_e32 v30, v28
	v_div_scale_f32 v29, vcc, s5, v25, s5
	v_fma_f32 v31, -v28, v30, 1.0
	v_fmac_f32_e32 v30, v31, v30
	v_mul_f32_e32 v31, v29, v30
	v_fma_f32 v32, -v28, v31, v29
	v_fmac_f32_e32 v31, v32, v30
	v_fma_f32 v28, -v28, v31, v29
	v_div_fmas_f32 v28, v28, v30, v31
	v_div_fixup_f32 v25, v28, v25, s5
	v_mul_f32_e32 v27, v27, v25
	v_mul_f32_e32 v22, v22, v25
	v_mul_f32_e32 v24, v24, v25
	v_mul_f32_e32 v23, v23, v25
	v_mul_f32_e32 v25, v0, v27
	v_mul_f32_e32 v22, v1, v22
	v_cvt_pk_fp8_f32 v26, v25, v22
	v_mul_f32_e32 v24, v2, v24
	v_mul_f32_e32 v23, v3, v23
	v_cvt_pk_fp8_f32 v26, v24, v23 op_sel:[0,0,1]
	global_store_dword v[8:9], v26, off offset:1536
	v_mov_b32_e32 v10, 0
	s_waitcnt vmcnt(4)
	v_lshlrev_b32_e32 v11, 16, v52
	s_waitcnt vmcnt(3)
	v_lshlrev_b32_e32 v26, 16, v54
	v_and_b32_e32 v22, 0xffff0000, v52
	v_and_b32_e32 v24, 0xffff0000, v54
	v_lshlrev_b32_e32 v27, 16, v53
	v_lshlrev_b32_e32 v28, 16, v55
	v_and_b32_e32 v23, 0xffff0000, v53
	v_and_b32_e32 v25, 0xffff0000, v55
	v_fma_f32 v22, -v19, v24, v22
	v_fma_f32 v23, -v19, v25, v23
	v_fma_f32 v11, -v19, v26, v11
	v_fma_f32 v24, -v19, v28, v27
	v_mul_f32_e32 v25, v22, v22
	v_mul_f32_e32 v26, v23, v23
	v_fmac_f32_e32 v25, v11, v11
	v_fmac_f32_e32 v26, v24, v24
	v_add_f32_e32 v25, v25, v26
	ds_bpermute_b32 v26, v13, v25
	s_waitcnt lgkmcnt(0)
	v_add_f32_e32 v25, v25, v26
	ds_bpermute_b32 v26, v14, v25
	s_waitcnt lgkmcnt(0)
	v_add_f32_e32 v25, v25, v26
	ds_bpermute_b32 v26, v15, v25
	s_waitcnt lgkmcnt(0)
	v_add_f32_e32 v25, v25, v26
	ds_bpermute_b32 v26, v16, v25
	s_waitcnt lgkmcnt(0)
	v_add_f32_e32 v25, v25, v26
	ds_bpermute_b32 v26, v17, v25
	s_waitcnt lgkmcnt(0)
	v_add_f32_e32 v25, v25, v26
	ds_bpermute_b32 v26, v18, v25
	s_waitcnt lgkmcnt(0)
	v_add_f32_e32 v25, v25, v26
	v_fmamk_f32 v25, v25, 0x3b800000, v20
	v_mul_f32_e32 v26, 0x4f800000, v25
	v_cmp_gt_f32_e32 vcc, s3, v25
	s_nop 1
	v_cndmask_b32_e32 v25, v25, v26, vcc
	v_sqrt_f32_e32 v26, v25
	s_nop 0
	v_add_u32_e32 v27, -1, v26
	v_add_u32_e32 v28, 1, v26
	v_fma_f32 v29, -v27, v26, v25
	v_fma_f32 v30, -v28, v26, v25
	v_cmp_ge_f32_e64 s[0:1], 0, v29
	s_nop 1
	v_cndmask_b32_e64 v26, v26, v27, s[0:1]
	v_cmp_lt_f32_e64 s[0:1], 0, v30
	s_nop 1
	v_cndmask_b32_e64 v26, v26, v28, s[0:1]
	v_mul_f32_e32 v27, 0x37800000, v26
	v_cndmask_b32_e32 v26, v26, v27, vcc
	v_cmp_class_f32_e32 vcc, v25, v21
	s_nop 1
	v_cndmask_b32_e32 v25, v26, v25, vcc
	v_div_scale_f32 v26, s[0:1], v25, v25, s5
	v_rcp_f32_e32 v28, v26
	v_div_scale_f32 v27, vcc, s5, v25, s5
	v_fma_f32 v29, -v26, v28, 1.0
	v_fmac_f32_e32 v28, v29, v28
	v_mul_f32_e32 v29, v27, v28
	v_fma_f32 v30, -v26, v29, v27
	v_fmac_f32_e32 v29, v30, v28
	v_fma_f32 v26, -v26, v29, v27
	v_div_fmas_f32 v26, v26, v28, v29
	v_div_fixup_f32 v25, v26, v25, s5
	v_mul_f32_e32 v11, v11, v25
	v_mul_f32_e32 v22, v22, v25
	v_mul_f32_e32 v11, v0, v11
	v_mul_f32_e32 v22, v1, v22
	v_cvt_pk_fp8_f32 v10, v11, v22
	v_mul_f32_e32 v24, v24, v25
	v_mul_f32_e32 v11, v23, v25
	v_mul_f32_e32 v22, v2, v24
	v_mul_f32_e32 v11, v3, v11
	v_cvt_pk_fp8_f32 v10, v22, v11 op_sel:[0,0,1]
	global_store_dword v[8:9], v10, off offset:1792
	s_cbranch_scc1 .LBB0_1817
